# E11 plus inline 0.0 addend for the last pixel first-vertex FMAs (one VALU fewer per wave)
# baseline (speedup 1.0000x reference)
.Lwarm_skip:
	s_or_b64 exec, exec, s[10:11]
	v_mad_u64_u32 v[2:3], s[6:7], v71, 12, s[6:7]
	v_lshlrev_b32_e32 v4, 2, v71
	v_mov_b32_e32 v5, v69
	s_movk_i32 s6, 0xfe00
	v_lshl_add_u64 v[4:5], s[8:9], 0, v[4:5]
	v_lshl_add_u64 v[8:9], v[2:3], 0, v[6:7]
	s_mov_b32 s7, -1
	v_lshl_add_u64 v[4:5], v[4:5], 0, v[6:7]
	v_lshl_add_u64 v[2:3], v[8:9], 0, s[6:7]
	v_cmp_gt_u32_e32 vcc, 32, v1
	v_lshlrev_b32_e32 v33, 12, v10
	v_add_u32_e32 v34, v33, v6
	v_cndmask_b32_e32 v3, v3, v5, vcc
	v_cndmask_b32_e32 v2, v2, v4, vcc
	global_load_dwordx4 v[2:5], v[2:3], off
	v_and_b32_e32 v72, 1, v0
	v_lshl_add_u32 v0, v32, 4, v33
	v_lshlrev_b32_e32 v73, 4, v32
	v_lshlrev_b32_e32 v74, 6, v72
	v_xor_b32_e32 v73, v73, v74
	v_lshl_add_u32 v73, v72, 11, v73
	v_lshl_add_u32 v73, v10, 12, v73
	v_and_b32_e32 v74, 31, v1
	v_lshrrev_b32_e32 v75, 5, v1
	v_lshl_or_b32 v76, v74, 2, v71
	v_lshlrev_b32_e32 v74, 4, v74
	v_lshlrev_b32_e32 v77, 6, v75
	v_xor_b32_e32 v74, v74, v77
	v_lshl_add_u32 v74, v75, 11, v74
	v_lshl_add_u32 v74, v10, 12, v74
	v_lshlrev_b32_e32 v77, 7, v71
	v_and_b32_e32 v77, 0xe000000, v77
	v_and_b32_e32 v76, 0x3fffc, v76
	v_lshlrev_b32_e32 v75, 21, v75
	v_or3_b32 v75, v77, v75, v76
	v_lshlrev_b32_e32 v75, 2, v75
	s_mul_i32 s6, s4, 0x138800
	s_mul_hi_i32 s5, s4, 0x138800
	s_add_u32 s2, s2, s6
	s_addc_u32 s3, s3, s5
	global_load_dwordx4 v[28:31], v[8:9], off offset:512
	s_waitcnt vmcnt(1)
	ds_write_b128 v34, v[2:5]
	ds_read_b128 v[4:7], v0
	v_lshlrev_b32_e32 v0, 4, v72
	s_waitcnt lgkmcnt(0)
	v_max_i32_e32 v1, 0, v4
	v_max_i32_e32 v2, 0, v5
	v_max_i32_e32 v3, 0, v6
	v_max_i32_e32 v8, 0, v7
	v_lshl_or_b32 v35, v1, 7, v0
	v_lshl_or_b32 v36, v2, 7, v0
	v_lshl_or_b32 v37, v3, 7, v0
	v_lshl_or_b32 v38, v8, 7, v0
	global_load_dwordx4 v[20:23], v35, s[2:3]
	global_load_dwordx4 v[16:19], v35, s[2:3] offset:32
	global_load_dwordx4 v[8:11], v35, s[2:3] offset:64
	global_load_dwordx4 v[64:67], v36, s[2:3]
	global_load_dwordx4 v[60:63], v36, s[2:3] offset:32
	global_load_dwordx4 v[56:59], v36, s[2:3] offset:64
	global_load_dwordx4 v[52:55], v37, s[2:3]
	global_load_dwordx4 v[48:51], v37, s[2:3] offset:32
	global_load_dwordx4 v[44:47], v37, s[2:3] offset:64
	global_load_dwordx4 v[24:27], v38, s[2:3]
	global_load_dwordx4 v[12:15], v38, s[2:3] offset:32
	global_load_dwordx4 v[0:3], v38, s[2:3] offset:64
	s_waitcnt vmcnt(12)
	ds_write_b128 v34, v[28:31] offset:1024
	v_mul_u32_u24_e32 v28, 48, v32
	v_cmp_lt_i32_e32 vcc, -1, v4
	v_add_u32_e32 v31, v33, v28
	v_mov_b32_e32 v28, 0
	s_and_saveexec_b64 s[2:3], vcc
	ds_read_b32 v28, v31 offset:512
	s_or_b64 exec, exec, s[2:3]
	s_and_saveexec_b64 s[2:3], vcc
	ds_read_b32 v69, v31 offset:516
	s_or_b64 exec, exec, s[2:3]
	v_mov_b32_e32 v29, 0
	v_mov_b32_e32 v4, 0
	s_and_saveexec_b64 s[2:3], vcc
	ds_read_b32 v4, v31 offset:520
	s_or_b64 exec, exec, s[2:3]
	s_waitcnt vmcnt(11) lgkmcnt(0)
	v_fma_mix_f32 v30, v28, v20, v29 op_sel_hi:[0,1,0]
	v_fma_mix_f32 v20, v28, v20, v29 op_sel:[0,1,0] op_sel_hi:[0,1,0]
	v_fma_mix_f32 v32, v28, v21, v29 op_sel_hi:[0,1,0]
	v_fma_mix_f32 v21, v28, v21, v29 op_sel:[0,1,0] op_sel_hi:[0,1,0]
	v_fma_mix_f32 v33, v28, v22, v29 op_sel_hi:[0,1,0]
	v_fma_mix_f32 v22, v28, v22, v29 op_sel:[0,1,0] op_sel_hi:[0,1,0]
	v_fma_mix_f32 v34, v28, v23, v29 op_sel_hi:[0,1,0]
	v_fma_mix_f32 v23, v28, v23, v29 op_sel:[0,1,0] op_sel_hi:[0,1,0]
	s_waitcnt vmcnt(10)
	v_fma_mix_f32 v28, v69, v16, v30 op_sel_hi:[0,1,0]
	v_fma_mix_f32 v16, v69, v16, v20 op_sel:[0,1,0] op_sel_hi:[0,1,0]
	v_fma_mix_f32 v20, v69, v17, v32 op_sel_hi:[0,1,0]
	v_cmp_lt_i32_e32 vcc, -1, v5
	v_fma_mix_f32 v17, v69, v17, v21 op_sel:[0,1,0] op_sel_hi:[0,1,0]
	v_fma_mix_f32 v21, v69, v18, v33 op_sel_hi:[0,1,0]
	v_fma_mix_f32 v18, v69, v18, v22 op_sel:[0,1,0] op_sel_hi:[0,1,0]
	v_fma_mix_f32 v22, v69, v19, v34 op_sel_hi:[0,1,0]
	v_fma_mix_f32 v19, v69, v19, v23 op_sel:[0,1,0] op_sel_hi:[0,1,0]
	s_waitcnt vmcnt(9)
	s_and_saveexec_b64 s[2:3], vcc
	ds_read_b32 v29, v31 offset:524
	s_or_b64 exec, exec, s[2:3]
	v_mov_b32_e32 v5, 0
	s_and_saveexec_b64 s[2:3], vcc
	ds_read_b32 v5, v31 offset:532
	s_or_b64 exec, exec, s[2:3]
	v_fma_mix_f32 v40, v4, v8, v28 op_sel_hi:[0,1,0]
	v_fma_mix_f32 v36, v4, v8, v16 op_sel:[0,1,0] op_sel_hi:[0,1,0]
	v_fma_mix_f32 v32, v4, v9, v20 op_sel_hi:[0,1,0]
	v_fma_mix_f32 v28, v4, v9, v17 op_sel:[0,1,0] op_sel_hi:[0,1,0]
	v_mov_b32_e32 v9, 0
	s_and_saveexec_b64 s[2:3], vcc
	ds_read_b32 v9, v31 offset:528
	s_or_b64 exec, exec, s[2:3]
	v_fma_mix_f32 v20, v4, v10, v21 op_sel_hi:[0,1,0]
	v_fma_mix_f32 v16, v4, v10, v18 op_sel:[0,1,0] op_sel_hi:[0,1,0]
	v_fma_mix_f32 v8, v4, v11, v22 op_sel_hi:[0,1,0]
	v_fma_mix_f32 v4, v4, v11, v19 op_sel:[0,1,0] op_sel_hi:[0,1,0]
	v_mov_b32_e32 v10, 0
	s_waitcnt vmcnt(8) lgkmcnt(0)
	v_fma_mix_f32 v18, v29, v65, v10 op_sel_hi:[0,1,0]
	v_fma_mix_f32 v17, v29, v64, v10 op_sel:[0,1,0] op_sel_hi:[0,1,0]
	v_fma_mix_f32 v21, v29, v66, v10 op_sel_hi:[0,1,0]
	v_fma_mix_f32 v11, v29, v64, v10 op_sel_hi:[0,1,0]
	v_fma_mix_f32 v19, v29, v65, v10 op_sel:[0,1,0] op_sel_hi:[0,1,0]
	s_waitcnt vmcnt(7)
	v_fma_mix_f32 v18, v9, v61, v18 op_sel_hi:[0,1,0]
	v_fma_mix_f32 v22, v29, v66, v10 op_sel:[0,1,0] op_sel_hi:[0,1,0]
	v_fma_mix_f32 v23, v29, v67, v10 op_sel_hi:[0,1,0]
	v_fma_mix_f32 v29, v29, v67, v10 op_sel:[0,1,0] op_sel_hi:[0,1,0]
	v_fma_mix_f32 v17, v9, v60, v17 op_sel:[0,1,0] op_sel_hi:[0,1,0]
	v_fma_mix_f32 v21, v9, v62, v21 op_sel_hi:[0,1,0]
	s_waitcnt vmcnt(6)
	v_fma_mix_f32 v33, v5, v57, v18 op_sel_hi:[0,1,0]
	v_cmp_lt_i32_e32 vcc, -1, v6
	v_mov_b32_e32 v18, 0
	s_and_saveexec_b64 s[2:3], vcc
	ds_read_b32 v18, v31 offset:536
	s_or_b64 exec, exec, s[2:3]
	s_and_saveexec_b64 s[2:3], vcc
	ds_read_b32 v10, v31 offset:540
	s_or_b64 exec, exec, s[2:3]
	v_mov_b32_e32 v6, 0
	s_and_saveexec_b64 s[2:3], vcc
	ds_read_b32 v6, v31 offset:544
	s_or_b64 exec, exec, s[2:3]
	v_fma_mix_f32 v11, v9, v60, v11 op_sel_hi:[0,1,0]
	v_fma_mix_f32 v19, v9, v61, v19 op_sel:[0,1,0] op_sel_hi:[0,1,0]
	v_fma_mix_f32 v22, v9, v62, v22 op_sel:[0,1,0] op_sel_hi:[0,1,0]
	v_fma_mix_f32 v23, v9, v63, v23 op_sel_hi:[0,1,0]
	v_fma_mix_f32 v30, v9, v63, v29 op_sel:[0,1,0] op_sel_hi:[0,1,0]
	v_fma_mix_f32 v37, v5, v56, v17 op_sel:[0,1,0] op_sel_hi:[0,1,0]
	s_nop 0
	v_fma_mix_f32 v41, v5, v56, v11 op_sel_hi:[0,1,0]
	v_fma_mix_f32 v29, v5, v57, v19 op_sel:[0,1,0] op_sel_hi:[0,1,0]
	v_fma_mix_f32 v21, v5, v58, v21 op_sel_hi:[0,1,0]
	v_fma_mix_f32 v17, v5, v58, v22 op_sel:[0,1,0] op_sel_hi:[0,1,0]
	v_fma_mix_f32 v9, v5, v59, v23 op_sel_hi:[0,1,0]
	v_fma_mix_f32 v5, v5, v59, v30 op_sel:[0,1,0] op_sel_hi:[0,1,0]
	v_mov_b32_e32 v11, 0
	s_waitcnt vmcnt(5) lgkmcnt(0)
	v_fma_mix_f32 v22, v18, v52, v11 op_sel:[0,1,0] op_sel_hi:[0,1,0]
	v_fma_mix_f32 v30, v18, v53, v11 op_sel:[0,1,0] op_sel_hi:[0,1,0]
	v_fma_mix_f32 v19, v18, v52, v11 op_sel_hi:[0,1,0]
	v_fma_mix_f32 v23, v18, v53, v11 op_sel_hi:[0,1,0]
	v_fma_mix_f32 v34, v18, v54, v11 op_sel_hi:[0,1,0]
	v_fma_mix_f32 v35, v18, v54, v11 op_sel:[0,1,0] op_sel_hi:[0,1,0]
	v_fma_mix_f32 v38, v18, v55, v11 op_sel_hi:[0,1,0]
	v_fma_mix_f32 v18, v18, v55, v11 op_sel:[0,1,0] op_sel_hi:[0,1,0]
	s_waitcnt vmcnt(4)
	v_fma_mix_f32 v22, v10, v48, v22 op_sel:[0,1,0] op_sel_hi:[0,1,0]
	v_fma_mix_f32 v30, v10, v49, v30 op_sel:[0,1,0] op_sel_hi:[0,1,0]
	v_cmp_lt_i32_e32 vcc, -1, v7
	s_and_saveexec_b64 s[2:3], vcc
	ds_read_b32 v11, v31 offset:548
	s_or_b64 exec, exec, s[2:3]
	v_mov_b32_e32 v7, 0
	s_and_saveexec_b64 s[2:3], vcc
	ds_read_b32 v7, v31 offset:556
	s_or_b64 exec, exec, s[2:3]
	v_fma_mix_f32 v19, v10, v48, v19 op_sel_hi:[0,1,0]
	v_fma_mix_f32 v23, v10, v49, v23 op_sel_hi:[0,1,0]
	v_fma_mix_f32 v39, v10, v50, v34 op_sel_hi:[0,1,0]
	v_fma_mix_f32 v35, v10, v50, v35 op_sel:[0,1,0] op_sel_hi:[0,1,0]
	v_fma_mix_f32 v43, v10, v51, v38 op_sel_hi:[0,1,0]
	v_fma_mix_f32 v48, v10, v51, v18 op_sel:[0,1,0] op_sel_hi:[0,1,0]
	s_waitcnt vmcnt(3)
	v_fma_mix_f32 v42, v6, v44, v19 op_sel_hi:[0,1,0]
	v_mov_b32_e32 v19, 0
	s_and_saveexec_b64 s[2:3], vcc
	ds_read_b32 v19, v31 offset:552
	s_or_b64 exec, exec, s[2:3]
	v_fma_mix_f32 v38, v6, v44, v22 op_sel:[0,1,0] op_sel_hi:[0,1,0]
	v_fma_mix_f32 v34, v6, v45, v23 op_sel_hi:[0,1,0]
	v_fma_mix_f32 v30, v6, v45, v30 op_sel:[0,1,0] op_sel_hi:[0,1,0]
	v_fma_mix_f32 v22, v6, v46, v39 op_sel_hi:[0,1,0]
	v_fma_mix_f32 v18, v6, v46, v35 op_sel:[0,1,0] op_sel_hi:[0,1,0]
	v_fma_mix_f32 v10, v6, v47, v43 op_sel_hi:[0,1,0]
	v_fma_mix_f32 v6, v6, v47, v48 op_sel:[0,1,0] op_sel_hi:[0,1,0]
	s_load_dwordx2 s[0:1], s[0:1], 0x18
	s_ashr_i32 s5, s4, 31
	s_waitcnt vmcnt(2) lgkmcnt(0)
	v_fma_mix_f32 v31, v11, v24, 0 op_sel_hi:[0,1,0]
	v_fma_mix_f32 v24, v11, v24, 0 op_sel:[0,1,0] op_sel_hi:[0,1,0]
	v_fma_mix_f32 v35, v11, v25, 0 op_sel_hi:[0,1,0]
	v_fma_mix_f32 v25, v11, v25, 0 op_sel:[0,1,0] op_sel_hi:[0,1,0]
	v_fma_mix_f32 v39, v11, v26, 0 op_sel_hi:[0,1,0]
	v_fma_mix_f32 v26, v11, v26, 0 op_sel:[0,1,0] op_sel_hi:[0,1,0]
	v_fma_mix_f32 v43, v11, v27, 0 op_sel_hi:[0,1,0]
	v_fma_mix_f32 v11, v11, v27, 0 op_sel:[0,1,0] op_sel_hi:[0,1,0]
	s_waitcnt vmcnt(1)
	v_fma_mix_f32 v23, v19, v12, v31 op_sel_hi:[0,1,0]
	s_lshl_b64 s[2:3], s[4:5], 24
	v_fma_mix_f32 v12, v19, v12, v24 op_sel:[0,1,0] op_sel_hi:[0,1,0]
	v_fma_mix_f32 v24, v19, v13, v35 op_sel_hi:[0,1,0]
	v_fma_mix_f32 v13, v19, v13, v25 op_sel:[0,1,0] op_sel_hi:[0,1,0]
	v_fma_mix_f32 v25, v19, v14, v39 op_sel_hi:[0,1,0]
	v_fma_mix_f32 v14, v19, v14, v26 op_sel:[0,1,0] op_sel_hi:[0,1,0]
	v_fma_mix_f32 v26, v19, v15, v43 op_sel_hi:[0,1,0]
	v_fma_mix_f32 v15, v19, v15, v11 op_sel:[0,1,0] op_sel_hi:[0,1,0]
	s_add_u32 s0, s0, s2
	s_addc_u32 s1, s1, s3
	s_add_u32 s2, s0, 0x100000
	s_addc_u32 s3, s1, 0
	s_add_u32 s4, s0, 0x200000
	s_addc_u32 s5, s1, 0
	s_add_u32 s6, s0, 0x300000
	s_addc_u32 s7, s1, 0
	s_add_u32 s8, s0, 0x400000
	s_addc_u32 s9, s1, 0
	s_add_u32 s10, s0, 0x500000
	s_addc_u32 s11, s1, 0
	s_add_u32 s12, s0, 0x600000
	s_addc_u32 s13, s1, 0
	s_add_u32 s14, s0, 0x700000
	s_addc_u32 s15, s1, 0
	s_waitcnt vmcnt(0)
	v_fma_mix_f32 v43, v7, v0, v23 op_sel_hi:[0,1,0]
	v_fma_mix_f32 v23, v7, v2, v25 op_sel_hi:[0,1,0]
	v_fma_mix_f32 v19, v7, v2, v14 op_sel:[0,1,0] op_sel_hi:[0,1,0]
	v_fma_mix_f32 v39, v7, v0, v12 op_sel:[0,1,0] op_sel_hi:[0,1,0]
	v_fma_mix_f32 v35, v7, v1, v24 op_sel_hi:[0,1,0]
	v_fma_mix_f32 v31, v7, v1, v13 op_sel:[0,1,0] op_sel_hi:[0,1,0]
	v_fma_mix_f32 v11, v7, v3, v26 op_sel_hi:[0,1,0]
	v_fma_mix_f32 v7, v7, v3, v15 op_sel:[0,1,0] op_sel_hi:[0,1,0]
	ds_write_b128 v73, v[40:43]
	ds_write_b128 v73, v[36:39] offset:512
	ds_write_b128 v73, v[32:35] offset:1024
	ds_write_b128 v73, v[28:31] offset:1536
	ds_read_b128 v[44:47], v74
	ds_read_b128 v[48:51], v74 offset:512
	ds_read_b128 v[52:55], v74 offset:1024
	ds_read_b128 v[56:59], v74 offset:1536
	ds_write_b128 v73, v[20:23]
	ds_write_b128 v73, v[16:19] offset:512
	ds_write_b128 v73, v[8:11] offset:1024
	ds_write_b128 v73, v[4:7] offset:1536
	s_waitcnt lgkmcnt(7)
	global_store_dwordx4 v75, v[44:47], s[0:1] nt
	s_waitcnt lgkmcnt(6)
	global_store_dwordx4 v75, v[48:51], s[2:3] nt
	s_waitcnt lgkmcnt(5)
	global_store_dwordx4 v75, v[52:55], s[4:5] nt
	s_waitcnt lgkmcnt(4)
	global_store_dwordx4 v75, v[56:59], s[6:7] nt
	ds_read_b128 v[60:63], v74
	ds_read_b128 v[64:67], v74 offset:512
	ds_read_b128 v[0:3], v74 offset:1024
	ds_read_b128 v[12:15], v74 offset:1536
	s_waitcnt lgkmcnt(3)
	global_store_dwordx4 v75, v[60:63], s[8:9] nt
	s_waitcnt lgkmcnt(2)
	global_store_dwordx4 v75, v[64:67], s[10:11] nt
	s_waitcnt lgkmcnt(1)
	global_store_dwordx4 v75, v[0:3], s[12:13] nt
	s_waitcnt lgkmcnt(0)
	global_store_dwordx4 v75, v[12:15], s[14:15] nt
	s_endpgm
